# P7/P8 unit loops: expert tile/row prefixes taken from the same per-lane LDS batch through v_readlane (two fewer dependent LDS round trips per unit)
# speedup vs baseline: 1.0115x; 1.0027x over previous
.LBB0_1203:
	s_mov_b64 s[74:75], 0
	s_and_b64 vcc, exec, s[0:1]
	s_cbranch_vccz .LBB0_1206
	s_cmp_ge_i32 s22, s24
	s_cbranch_scc1 .LBB0_1206
	s_ashr_i32 s0, s22, 31
	s_lshr_b32 s0, s0, 29
	s_add_i32 s0, s22, s0
	s_ashr_i32 s0, s0, 3
	s_mov_b64 s[74:75], -1
	v_mbcnt_lo_u32_b32 v2, -1, 0
	v_mbcnt_hi_u32_b32 v2, -1, v2
	v_min_u32_e32 v2, 32, v2
	v_lshlrev_b32_e32 v2, 2, v2
	v_add_u32_e32 v134, 0x20400, v2
	v_add_u32_e32 v2, 0x20490, v2
	ds_read_b32 v134, v134
	ds_read_b32 v2, v2
	s_waitcnt lgkmcnt(0)
	v_cmp_ge_i32_e32 vcc, s0, v2
	s_and_b32 s64, vcc_lo, 0xfffffffe
	s_bcnt1_i32_b32 s64, s64
	s_add_i32 s1, s64, 1
	v_readlane_b32 s6, v2, s64
	v_readlane_b32 s7, v134, s1
	v_readlane_b32 s1, v134, s64
	s_sub_i32 s6, s0, s6
	s_lshl_b32 s6, s6, 8
	s_sub_i32 s0, s64, s0
	s_lshl_b32 s0, s0, 11
	s_add_i32 s13, s1, s6
	s_sub_i32 s1, s7, s13
	s_min_i32 s12, s1, 0x100
	s_lshl_b32 s1, s22, 8
	s_add_i32 s82, s0, s1
	s_lshl_b32 s0, s64, 14
	s_add_i32 s70, s6, s0

.LBB0_1307:
	s_mov_b64 s[0:1], -1
	s_and_b64 vcc, exec, s[2:3]
	s_cbranch_vccz .LBB0_1310
	s_cmp_ge_i32 s4, s34
	s_cbranch_scc1 .LBB0_1310
	s_ashr_i32 s0, s4, 31
	s_lshr_b32 s0, s0, 30
	s_add_i32 s0, s4, s0
	s_ashr_i32 s0, s0, 2
	v_mbcnt_lo_u32_b32 v0, -1, 0
	v_mbcnt_hi_u32_b32 v0, -1, v0
	v_min_u32_e32 v0, 32, v0
	v_lshlrev_b32_e32 v0, 2, v0
	v_add_u32_e32 v2, 0x20400, v0
	v_add_u32_e32 v0, 0x20490, v0
	ds_read_b32 v2, v2
	ds_read_b32 v0, v0
	s_waitcnt lgkmcnt(0)
	v_cmp_ge_i32_e32 vcc, s0, v0
	s_and_b32 s46, vcc_lo, 0xfffffffe
	s_bcnt1_i32_b32 s46, s46
	s_add_i32 s2, s46, 1
	v_readlane_b32 s1, v0, s46
	v_readlane_b32 s3, v2, s2
	v_readlane_b32 s2, v2, s46
	s_sub_i32 s1, s0, s1
	s_lshl_b32 s1, s1, 8
	s_add_i32 s80, s2, s1
	s_sub_i32 s1, s3, s80
	s_sub_i32 s0, s46, s0
	s_min_i32 s79, s1, 0x100
	s_lshl_b32 s0, s0, 10
	s_lshl_b32 s1, s4, 8
	s_add_i32 s63, s0, s1
	s_mov_b64 s[0:1], 0
